# z_setup: loads into unused registers, its wait / LDS writes / barrier moved behind the first unit's z_load block so the two round trips overlap
# baseline (speedup 1.0000x reference)
; #define LAS __attribute__((address_space(3)))
; __device__ __forceinline__ void prefetch(Pre& P, const bf16_t* proj, const float* gates, size_t rb, int c, int h, int tid, int lane) {
;     const int cc = tid & 31, rg = tid >> 5;
;     const int col = (cc < 16) ? (C_LQ + h * 128 + 8 * cc) : (C_LK + h * 128 + 8 * (cc - 16));
; #pragma unroll
;     for (int i = 0; i < 7; ++i) { const int pos = c * 64 + 4 * rg - 3 + i;
;         if (pos >= 0) P.raw[i] = *(const u32x4*)(proj + (rb + pos) * NIN + col); else P.raw[i] = (u32x4){0u, 0u, 0u, 0u}; }
; __device__ __forceinline__ void z_setup(Frame& F, const float* conv_w, const float* conv_b, const float* normw) {
;     __syncthreads();
;     for (int i = F.tid; i < 5 * 1024; i += NTHR) { const int j = i >> 10, ch = i & 1023; ((LAS float*)(F.lds + ZCW))[i] = (j < 4) ? conv_w[j * 1024 + ch] : conv_b[ch]; }
;     ((LAS float*)(F.lds + ZNW))[F.tid] = normw[F.tid];
;     __syncthreads();
.LBB0_645:
	s_mov_b64 s[8:9], 0x1000
	v_lshl_add_u64 v[10:11], v[4:5], 0, s[8:9]
	v_lshl_add_u64 v[12:13], v[10:11], 0, s[8:9]
	v_lshl_add_u64 v[14:15], v[12:13], 0, s[8:9]
	v_lshl_add_u64 v[16:17], s[6:7], 0, v[2:3]
	global_load_dword v230, v[4:5], off
	global_load_dword v231, v[4:5], off offset:2048
	global_load_dword v232, v[10:11], off
	global_load_dword v233, v[10:11], off offset:2048
	global_load_dword v234, v[12:13], off
	global_load_dword v235, v[12:13], off offset:2048
	global_load_dword v236, v[14:15], off
	global_load_dword v237, v[14:15], off offset:2048
	global_load_dword v238, v[16:17], off
	global_load_dword v239, v[16:17], off offset:2048
	v_mov_b32_e32 v34, 0
	v_lshlrev_b32_e32 v110, 2, v0
	v_mov_b32_e32 v111, v34
	v_lshl_add_u64 v[2:3], s[0:1], 0, v[110:111]
	global_load_dword v240, v[2:3], off
	v_mov_b32_e32 v241, v1
	v_lshl_add_u32 v242, v0, 2, 0
	s_cmpk_lt_i32 s2, 0x400
	v_add_u32_e32 v242, 0x1f300, v242
	s_cselect_b64 s[0:1], -1, 0
	s_cmpk_gt_i32 s2, 0x3ff
	s_cbranch_scc1 .LBB0_656
	s_ashr_i32 s3, s2, 5
	s_and_b32 s4, s3, 3
	v_and_b32_e32 v1, 31, v0
	s_lshl_b32 s11, s4, 7
	v_lshlrev_b32_e32 v2, 3, v1
	v_or_b32_e32 v3, s11, v2
	v_add_u32_e32 v2, s11, v2
	s_lshl_b32 s8, s2, 6
	v_or_b32_e32 v3, 0x600, v3
	v_add_u32_e32 v2, 0x780, v2
	v_cmp_gt_u32_e32 vcc, 16, v1
	s_ashr_i32 s6, s2, 7
	s_and_b32 s10, s8, 0x7c0
	v_lshrrev_b32_e32 v8, 5, v0
	v_cndmask_b32_e32 v3, v2, v3, vcc
	s_ashr_i32 s7, s6, 31
	v_lshl_or_b32 v2, v8, 2, s10
	v_lshlrev_b32_e32 v4, 1, v3
	v_mov_b32_e32 v5, v34
	s_lshl_b64 s[6:7], s[6:7], 11
	v_add_u32_e32 v6, -3, v2
	v_lshl_add_u64 v[4:5], s[58:59], 0, v[4:5]
	v_cmp_ne_u32_e32 vcc, 0, v2
	v_mov_b32_e32 v35, 0
	v_mov_b32_e32 v36, 0
	v_mov_b32_e32 v37, 0
	s_and_saveexec_b64 s[8:9], vcc
	s_cbranch_execz .LBB0_649
	v_mov_b32_e32 v7, 0
	v_lshl_add_u64 v[10:11], s[6:7], 0, v[6:7]
	s_movk_i32 s14, 0x2600
	v_mad_u64_u32 v[12:13], s[12:13], v10, s14, v[4:5]
	v_mad_i32_i24 v13, v11, s14, v13
	global_load_dwordx4 v[34:37], v[12:13], off

; #define LAS __attribute__((address_space(3)))
; __device__ __forceinline__ void z_setup(Frame& F, const float* conv_w, const float* conv_b, const float* normw) {
;     ...
;     for (int i = F.tid; i < 5 * 1024; i += NTHR) { const int j = i >> 10, ch = i & 1023; ((LAS float*)(F.lds + ZCW))[i] = (j < 4) ? conv_w[j * 1024 + ch] : conv_b[ch]; }
;     ((LAS float*)(F.lds + ZNW))[F.tid] = normw[F.tid];
;     __syncthreads();
; __device__ __forceinline__ void z_load(ZL& L, const Frame& F, const bf16_t* proj, const float* gates, const MW& W, int u) {
;     ...
;     L.npv = (tid < 128) ? W.NP[(size_t)u * 128 + tid] : 0.f; L.mprev = W.MP[u];
; #pragma unroll
;     for (int g = 0; g < 4; ++g) L.og[g] = *(const u32x2*)(proj + (r0 + trow) * NIN + C_LO + h * 128 + 32 * et + 8 * g + 4 * hh);
.LBB0_655:
	s_or_b64 exec, exec, s[6:7]
	v_readlane_b32 s13, v255, 9
	s_lshl_b32 s4, s13, 3
	s_and_b32 s4, s4, 0x1fffffe0
	s_lshl_b64 s[6:7], s[2:3], 2
	v_or_b32_e32 v2, s4, v1
	s_add_u32 s6, s64, s6
	s_addc_u32 s7, s65, s7
	v_lshl_add_u64 v[4:5], s[10:11], 0, v[2:3]
	v_mov_b64_e32 v[6:7], s[58:59]
	global_load_dword v165, v3, s[6:7]
	v_mad_u64_u32 v[6:7], s[6:7], v4, s12, v[6:7]
	v_mov_b32_e32 v2, v7
	v_mad_u64_u32 v[4:5], s[6:7], v5, s12, v[2:3]
	v_mov_b32_e32 v7, v4
	s_lshl_b32 s3, s13, 6
	v_lshl_add_u64 v[4:5], v[6:7], 0, s[8:9]
	s_and_b32 s8, s3, 0xc0
	v_lshrrev_b32_e32 v1, 2, v0
	v_lshl_add_u64 v[4:5], v[4:5], 0, s[8:9]
	v_and_b32_e32 v2, 8, v1
	v_lshl_add_u64 v[2:3], v[4:5], 0, v[2:3]
	s_mov_b64 s[6:7], 0x1800
	v_lshl_add_u64 v[4:5], v[2:3], 0, s[6:7]
	v_add_co_u32_e32 v2, vcc, 0x1000, v2
	s_nop 1
	v_addc_co_u32_e32 v3, vcc, 0, v3, vcc
	global_load_dwordx2 v[136:137], v[2:3], off offset:2048
	global_load_dwordx2 v[134:135], v[4:5], off offset:16
	global_load_dwordx2 v[132:133], v[4:5], off offset:32
	global_load_dwordx2 v[114:115], v[4:5], off offset:48
	s_waitcnt vmcnt(0)
	ds_write_b32 v241, v230
	ds_write_b32 v241, v231 offset:2048
	ds_write_b32 v241, v232 offset:4096
	ds_write_b32 v241, v233 offset:6144
	ds_write_b32 v241, v234 offset:8192
	ds_write_b32 v241, v235 offset:10240
	ds_write_b32 v241, v236 offset:12288
	ds_write_b32 v241, v237 offset:14336
	ds_write_b32 v241, v238 offset:16384
	ds_write_b32 v241, v239 offset:18432
	ds_write_b32 v242, v240
	s_waitcnt lgkmcnt(0)
	s_barrier
	s_andn2_b64 vcc, exec, s[0:1]
	s_cbranch_vccz .LBB0_657
	s_branch .LBB0_685
.LBB0_656:
	s_waitcnt vmcnt(0)
	ds_write_b32 v241, v230
	ds_write_b32 v241, v231 offset:2048
	ds_write_b32 v241, v232 offset:4096
	ds_write_b32 v241, v233 offset:6144
	ds_write_b32 v241, v234 offset:8192
	ds_write_b32 v241, v235 offset:10240
	ds_write_b32 v241, v236 offset:12288
	ds_write_b32 v241, v237 offset:14336
	ds_write_b32 v241, v238 offset:16384
	ds_write_b32 v241, v239 offset:18432
	ds_write_b32 v242, v240
	s_waitcnt lgkmcnt(0)
	s_barrier
	s_andn2_b64 vcc, exec, s[0:1]
	s_cbranch_vccnz .LBB0_685

; #define LAS __attribute__((address_space(3)))
; __device__ __forceinline__ void prefetch(Pre& P, const bf16_t* proj, const float* gates, size_t rb, int c, int h, int tid, int lane) {
;     const int cc = tid & 31, rg = tid >> 5;
;     const int col = (cc < 16) ? (C_LQ + h * 128 + 8 * cc) : (C_LK + h * 128 + 8 * (cc - 16));
; #pragma unroll
;     for (int i = 0; i < 7; ++i) { const int pos = c * 64 + 4 * rg - 3 + i;
;         if (pos >= 0) P.raw[i] = *(const u32x4*)(proj + (rb + pos) * NIN + col); else P.raw[i] = (u32x4){0u, 0u, 0u, 0u}; }
; __device__ __forceinline__ void z_setup(Frame& F, const float* conv_w, const float* conv_b, const float* normw) {
;     __syncthreads();
;     for (int i = F.tid; i < 5 * 1024; i += NTHR) { const int j = i >> 10, ch = i & 1023; ((LAS float*)(F.lds + ZCW))[i] = (j < 4) ? conv_w[j * 1024 + ch] : conv_b[ch]; }
;     ((LAS float*)(F.lds + ZNW))[F.tid] = normw[F.tid];
;     __syncthreads();
.LBB0_1773:
	s_mov_b64 s[8:9], 0x1000
	v_lshl_add_u64 v[10:11], v[4:5], 0, s[8:9]
	v_lshl_add_u64 v[12:13], v[10:11], 0, s[8:9]
	v_lshl_add_u64 v[14:15], v[12:13], 0, s[8:9]
	v_lshl_add_u64 v[16:17], s[0:1], 0, v[2:3]
	global_load_dword v230, v[4:5], off
	global_load_dword v231, v[4:5], off offset:2048
	global_load_dword v232, v[10:11], off
	global_load_dword v233, v[10:11], off offset:2048
	global_load_dword v234, v[12:13], off
	global_load_dword v235, v[12:13], off offset:2048
	global_load_dword v236, v[14:15], off
	global_load_dword v237, v[14:15], off offset:2048
	global_load_dword v238, v[16:17], off
	global_load_dword v239, v[16:17], off offset:2048
	v_mov_b32_e32 v34, 0
	v_lshlrev_b32_e32 v110, 2, v0
	v_mov_b32_e32 v111, v34
	v_lshl_add_u64 v[2:3], s[6:7], 0, v[110:111]
	global_load_dword v240, v[2:3], off offset:2048
	v_mov_b32_e32 v241, v1
	v_lshl_add_u32 v242, v0, 2, 0
	s_cmpk_lt_i32 s2, 0x400
	v_add_u32_e32 v242, 0x1f300, v242
	s_cselect_b64 s[0:1], -1, 0
	s_cmpk_gt_i32 s2, 0x3ff
	s_cbranch_scc1 .LBB0_1784
	s_ashr_i32 s3, s2, 5
	s_and_b32 s4, s3, 3
	s_lshl_b32 s11, s4, 7
	v_lshlrev_b32_e32 v2, 3, v203
	v_or_b32_e32 v3, s11, v2
	v_add_u32_e32 v2, s11, v2
	s_lshl_b32 s8, s2, 6
	v_or_b32_e32 v3, 0x600, v3
	v_add_u32_e32 v2, 0x780, v2
	v_cmp_gt_u32_e32 vcc, 16, v203
	s_ashr_i32 s6, s2, 7
	s_and_b32 s10, s8, 0x7c0
	v_lshrrev_b32_e32 v1, 5, v0
	v_cndmask_b32_e32 v3, v2, v3, vcc
	s_ashr_i32 s7, s6, 31
	v_lshl_or_b32 v2, v1, 2, s10
	v_lshlrev_b32_e32 v4, 1, v3
	v_mov_b32_e32 v5, v34
	s_lshl_b64 s[6:7], s[6:7], 11
	v_add_u32_e32 v6, -3, v2
	v_lshl_add_u64 v[4:5], s[58:59], 0, v[4:5]
	v_cmp_ne_u32_e32 vcc, 0, v2
	v_mov_b32_e32 v35, 0
	v_mov_b32_e32 v36, 0
	v_mov_b32_e32 v37, 0
	s_and_saveexec_b64 s[8:9], vcc
	s_cbranch_execz .LBB0_1777
	v_mov_b32_e32 v7, 0
	v_lshl_add_u64 v[8:9], s[6:7], 0, v[6:7]
	s_movk_i32 s14, 0x2600
	v_mad_u64_u32 v[10:11], s[12:13], v8, s14, v[4:5]
	v_mad_i32_i24 v11, v9, s14, v11
	global_load_dwordx4 v[34:37], v[10:11], off

; #define LAS __attribute__((address_space(3)))
; __device__ __forceinline__ void z_setup(Frame& F, const float* conv_w, const float* conv_b, const float* normw) {
;     ...
;     for (int i = F.tid; i < 5 * 1024; i += NTHR) { const int j = i >> 10, ch = i & 1023; ((LAS float*)(F.lds + ZCW))[i] = (j < 4) ? conv_w[j * 1024 + ch] : conv_b[ch]; }
;     ((LAS float*)(F.lds + ZNW))[F.tid] = normw[F.tid];
;     __syncthreads();
; __device__ __forceinline__ void z_load(ZL& L, const Frame& F, const bf16_t* proj, const float* gates, const MW& W, int u) {
;     ...
;     L.npv = (tid < 128) ? W.NP[(size_t)u * 128 + tid] : 0.f; L.mprev = W.MP[u];
; #pragma unroll
;     for (int g = 0; g < 4; ++g) L.og[g] = *(const u32x2*)(proj + (r0 + trow) * NIN + C_LO + h * 128 + 32 * et + 8 * g + 4 * hh);
.LBB0_1783:
	s_or_b64 exec, exec, s[6:7]
	v_readlane_b32 s13, v255, 9
	s_lshl_b32 s4, s13, 3
	s_and_b32 s4, s4, 0x1fffffe0
	s_lshl_b64 s[6:7], s[2:3], 2
	v_or_b32_e32 v2, s4, v203
	s_add_u32 s6, s64, s6
	s_addc_u32 s7, s65, s7
	v_lshl_add_u64 v[4:5], s[10:11], 0, v[2:3]
	v_mov_b64_e32 v[6:7], s[58:59]
	global_load_dword v166, v3, s[6:7]
	v_mad_u64_u32 v[6:7], s[6:7], v4, s12, v[6:7]
	v_mov_b32_e32 v2, v7
	v_mad_u64_u32 v[4:5], s[6:7], v5, s12, v[2:3]
	v_mov_b32_e32 v7, v4
	s_lshl_b32 s3, s13, 6
	v_lshl_add_u64 v[4:5], v[6:7], 0, s[8:9]
	s_and_b32 s8, s3, 0xc0
	v_lshrrev_b32_e32 v2, 2, v0
	v_lshl_add_u64 v[4:5], v[4:5], 0, s[8:9]
	v_and_b32_e32 v2, 8, v2
	v_lshl_add_u64 v[2:3], v[4:5], 0, v[2:3]
	s_mov_b64 s[6:7], 0x1800
	v_lshl_add_u64 v[4:5], v[2:3], 0, s[6:7]
	v_add_co_u32_e32 v2, vcc, 0x1000, v2
	s_nop 1
	v_addc_co_u32_e32 v3, vcc, 0, v3, vcc
	global_load_dwordx2 v[136:137], v[2:3], off offset:2048
	global_load_dwordx2 v[134:135], v[4:5], off offset:16
	global_load_dwordx2 v[132:133], v[4:5], off offset:32
	global_load_dwordx2 v[114:115], v[4:5], off offset:48
	s_waitcnt vmcnt(0)
	ds_write_b32 v241, v230
	ds_write_b32 v241, v231 offset:2048
	ds_write_b32 v241, v232 offset:4096
	ds_write_b32 v241, v233 offset:6144
	ds_write_b32 v241, v234 offset:8192
	ds_write_b32 v241, v235 offset:10240
	ds_write_b32 v241, v236 offset:12288
	ds_write_b32 v241, v237 offset:14336
	ds_write_b32 v241, v238 offset:16384
	ds_write_b32 v241, v239 offset:18432
	ds_write_b32 v242, v240
	s_waitcnt lgkmcnt(0)
	s_barrier
	s_andn2_b64 vcc, exec, s[0:1]
	s_cbranch_vccz .LBB0_1785
	s_branch .LBB0_1813
